# static priority for the younger wave half also in the gla_scan and router phases
# baseline (speedup 1.0000x reference)
.LBB0_825:
	s_cmpk_lt_i32 s96, 0x100
	v_mov_b32_e32 v2, v0
	s_cselect_b64 s[4:5], -1, 0
	s_cmpk_gt_i32 s96, 0xff
	s_movk_i32 s6, 0x100
	s_cbranch_scc1 .LBB0_839
	s_add_u32 s8, s84, 0x40600000
	s_addc_u32 s9, s85, 0
	s_add_u32 s10, s84, 0x11000000
	s_addc_u32 s11, s85, 0
	s_add_u32 s26, s84, 0x41000000
	v_readlane_b32 s18, v252, 6
	s_addc_u32 s27, s85, 0
	s_lshl_b32 s7, s18, 6
	s_add_u32 s14, s84, s7
	v_mov_b32_e32 v69, 0
	s_addc_u32 s15, s85, 0
	v_and_b32_e32 v66, 48, v2
	v_mov_b32_e32 v67, v69
	v_lshl_add_u64 v[4:5], s[14:15], 0, v[66:67]
	s_mov_b64 s[14:15], 0x40e00000
	s_lshl_b32 s16, s18, 3
	v_and_b32_e32 v7, 15, v2
	v_lshl_add_u64 v[70:71], v[4:5], 0, s[14:15]
	v_ashrrev_i32_e32 v3, 31, v2
	v_lshrrev_b32_e32 v11, 2, v2
	v_lshlrev_b32_e32 v13, 4, v2
	s_movk_i32 s14, 0x48
	v_readlane_b32 s17, v252, 0
	s_and_b32 s16, s16, 0x1ffffff0
	v_bfe_u32 v8, v2, 4, 2
	v_lshlrev_b64 v[4:5], 3, v[2:3]
	v_and_b32_e32 v13, 0xf0, v13
	v_ashrrev_i32_e32 v92, 3, v2
	s_movk_i32 s12, 0x90
	v_mul_lo_u32 v11, v11, s14
	v_lshl_add_u64 v[72:73], v[2:3], 4, s[8:9]
	s_bfe_u32 s15, s17, 0x10006
	v_or_b32_e32 v3, s16, v7
	v_lshlrev_b32_e32 v10, 2, v8
	v_add_u32_e32 v14, 0, v13
	v_mul_lo_u32 v13, v92, s12
	v_add_u32_e32 v17, 0, v11
	v_mul_lo_u32 v11, v3, s12
	v_lshlrev_b32_e32 v19, 3, v8
	s_lshl_b32 s12, s15, 5
	v_lshlrev_b32_e32 v8, 3, v2
	v_add_u32_e32 v15, 0, v13
	v_and_b32_e32 v13, 7, v2
	v_and_b32_e32 v8, 24, v8
	s_add_i32 s12, s12, 0
	v_add_u32_e32 v93, 0, v11
	v_add_u32_e32 v94, s12, v8
	v_add_u32_e32 v96, 0, v8
	v_or_b32_e32 v21, s16, v10
	v_mul_lo_u32 v11, v92, 36
	v_lshlrev_b32_e32 v8, 2, v13
	v_lshl_or_b32 v24, s18, 4, v10
	v_add_u32_e32 v10, 0x200, v2
	v_bfe_u32 v9, v2, 2, 2
	v_and_b32_e32 v12, 3, v2
	v_add_lshl_u32 v23, v11, v8, 2
	v_ashrrev_i32_e32 v11, 31, v10
	v_lshlrev_b32_e32 v6, 3, v12
	v_lshlrev_b32_e32 v16, 4, v13
	v_lshlrev_b32_e32 v18, 4, v12
	v_lshl_add_u32 v95, v3, 7, v93
	v_or_b32_e32 v3, v19, v9
	v_lshlrev_b64 v[12:13], 3, v[10:11]
	v_lshrrev_b32_e32 v11, 4, v2
	s_movk_i32 s12, 0x110
	v_lshrrev_b32_e32 v10, 4, v10
	v_or_b32_e32 v25, 32, v19
	v_or_b32_e32 v26, 64, v19
	v_or_b32_e32 v19, 0x60, v19
	v_mul_lo_u32 v11, v11, s12
	v_mul_lo_u32 v10, v10, s12
	v_mul_u32_u24_e32 v97, 0x48, v3
	v_lshlrev_b32_e32 v98, 1, v25
	v_or_b32_e32 v25, v25, v9
	v_lshlrev_b32_e32 v27, 1, v26
	v_or_b32_e32 v26, v26, v9
	v_lshlrev_b32_e32 v28, 1, v19
	v_or_b32_e32 v9, v19, v9
	v_mul_u32_u24_e32 v19, 0x110, v3
	v_or_b32_e32 v3, 32, v3
	s_and_b32 s12, s17, 0xffffffc0
	v_lshl_or_b32 v22, s15, 4, v7
	v_mul_u32_u24_e32 v29, 0x48, v3
	v_mul_lo_u32 v3, v21, 36
	v_mul_lo_u32 v24, v24, s14
	s_add_u32 s14, s84, s12
	s_movk_i32 s0, 0x900
	v_add_lshl_u32 v99, v3, v22, 2
	v_lshl_add_u32 v3, v2, 2, 0
	s_addc_u32 s15, s85, 0
	v_cmp_gt_i32_e64 s[0:1], s0, v2
	v_bfe_u32 v1, v2, 2, 6
	v_cmp_gt_i32_e64 s[6:7], s6, v2
	v_lshl_add_u32 v20, s18, 5, v96
	v_lshl_add_u32 v7, v7, 1, 0
	v_mul_u32_u24_e32 v25, 0x48, v25
	v_mul_u32_u24_e32 v26, 0x48, v26
	v_mul_u32_u24_e32 v9, 0x48, v9
	v_add_u32_e32 v21, 0x90, v99
	v_add_u32_e32 v22, 0x120, v99
	v_add_u32_e32 v30, 0x1b0, v99
	v_add_u32_e32 v100, 0xbe00, v3
	v_add_u32_e32 v101, 0xfffffe00, v2
	v_lshl_add_u64 v[2:3], s[14:15], 0, v[66:67]
	s_mov_b64 s[14:15], 0x40e00200
	s_mov_b32 s12, 0xac00
	s_mov_b32 s13, 0
	v_lshl_add_u64 v[74:75], v[2:3], 0, s[14:15]
	s_movk_i32 s28, 0x6ff
	v_lshlrev_b32_e32 v68, 1, v6
	s_movk_i32 s29, 0x2000
	v_lshlrev_b32_e32 v76, 2, v8
	s_mov_b64 s[14:15], 0x400
	v_lshlrev_b64 v[78:79], 1, v[4:5]
	v_lshlrev_b64 v[80:81], 1, v[12:13]
	v_add_u32_e32 v67, v14, v11
	v_add_u32_e32 v102, v14, v10
	v_add_u32_e32 v103, v15, v16
	v_add3_u32 v104, v17, v18, s12
	v_add_u32_e32 v105, v94, v25
	v_add_u32_e32 v106, v95, v27
	v_add_u32_e32 v107, v94, v26
	v_add_u32_e32 v108, v95, v28
	v_add_u32_e32 v109, v94, v9
	v_add_u32_e32 v110, v20, v19
	v_add_u32_e32 v111, v96, v29
	v_add_u32_e32 v112, 0, v21
	v_add_u32_e32 v113, 0, v22
	v_add_u32_e32 v114, 0, v30
	v_add_u32_e32 v115, 0, v23
	v_add_u32_e32 v116, v7, v24
	s_mov_b32 s30, s96
	s_cmpk_lg_i32 s43, 0x100
	s_cbranch_scc1 .Lmy_gs_nomap
	s_and_b32 s30, s96, 7
	s_lshl_b32 s30, s30, 2
	s_lshr_b32 s100, s96, 6
	s_add_i32 s30, s30, s100
	s_lshl_b32 s30, s30, 3
	s_bfe_u32 s100, s96, 0x30003
	s_add_i32 s30, s30, s100
.Lmy_gs_nomap:
	v_readfirstlane_b32 s101, v0
	s_nop 3
	s_lshr_b32 s101, s101, 8
	s_cmp_eq_u32 s101, 0
	s_cbranch_scc1 .Lmy_prio_gs
	s_setprio 1

.LBB0_839:
	s_setprio 0
	s_waitcnt vmcnt(0)
	s_waitcnt lgkmcnt(0)
	s_barrier
	s_mov_b64 s[0:1], exec
	v_readlane_b32 s6, v252, 4
	v_readlane_b32 s7, v252, 5
	s_and_b64 s[6:7], s[0:1], s[6:7]
	s_mov_b64 exec, s[6:7]
	s_cbranch_execz .LBB0_891
	s_add_i32 s6, 0, 0x22020
	v_mov_b32_e32 v1, s6
	s_waitcnt vmcnt(0) expcnt(0) lgkmcnt(0)
	ds_read_b32 v3, v1
	s_add_i32 s6, 0, 0x22024
	v_mov_b32_e32 v1, s6
	ds_read_b32 v1, v1
	s_waitcnt lgkmcnt(1)
	v_cmp_ne_u32_e32 vcc, 0, v3
	s_cbranch_vccnz .LBB0_855
	v_readlane_b32 s6, v252, 1
	v_readlane_b32 s7, v252, 2
	s_load_dwordx2 s[10:11], s[6:7], 0x4
	s_add_u32 s6, s84, 0x4200
	s_addc_u32 s7, s85, 0
	s_add_u32 s8, s84, 0x4400
	s_addc_u32 s9, s85, 0
	s_waitcnt lgkmcnt(0)
	s_mul_i32 s33, s10, s43
	s_add_u32 s10, s84, 0x4500
	s_mul_i32 s33, s33, s11
	s_addc_u32 s11, s85, 0
	s_add_u32 s12, s84, 0x4600
	s_addc_u32 s13, s85, 0
	s_add_u32 s14, s84, 0x4700
	s_addc_u32 s15, s85, 0
	s_add_u32 s16, s84, 0x4800
	s_addc_u32 s17, s85, 0
	s_add_u32 s18, s84, 0x4900
	s_addc_u32 s19, s85, 0
	s_add_u32 s20, s84, 0x4a00
	s_addc_u32 s21, s85, 0
	s_add_u32 s22, s84, 0x4b00
	s_addc_u32 s23, s85, 0
	s_add_u32 s24, s84, 0x4c00
	s_addc_u32 s25, s85, 0
	s_add_u32 s26, s84, 0x4d00
	s_addc_u32 s27, s85, 0
	s_add_u32 s28, s84, 0x4e00
	s_addc_u32 s29, s85, 0
	s_add_u32 s30, s84, 0x4f00
	s_addc_u32 s31, s85, 0
	s_add_u32 s34, s84, 0x5000
	s_addc_u32 s35, s85, 0
	s_add_u32 s36, s84, 0x5100
	s_addc_u32 s37, s85, 0
	s_add_u32 s38, s84, 0x5200
	s_addc_u32 s39, s85, 0
	s_add_u32 s40, s84, 0x5300
	s_addc_u32 s41, s85, 0
	s_mov_b32 s48, 1
	v_mov_b32_e32 v17, 0
	s_branch .LBB0_843

.LBB0_1164:
	s_or_b64 exec, exec, s[4:5]
	v_readlane_b32 s4, v251, 8
	s_add_u32 s18, s84, 0x45000000
	v_readlane_b32 s5, v251, 9
	v_mov_b32_e32 v2, v0
	s_addc_u32 s19, s85, 0
	s_and_b64 vcc, exec, s[4:5]
	s_waitcnt lgkmcnt(0)
	s_barrier
	s_cbranch_vccnz .LBB0_1266
	v_and_b32_e32 v6, 7, v2
	v_mbcnt_hi_u32_b32 v10, -1, v228
	v_lshlrev_b32_e32 v4, 4, v6
	v_mov_b32_e32 v5, 0
	v_and_b32_e32 v7, 64, v10
	v_lshl_add_u64 v[198:199], s[6:7], 0, v[4:5]
	v_xor_b32_e32 v4, 1, v10
	v_add_u32_e32 v11, 64, v7
	v_cmp_lt_i32_e32 vcc, v4, v11
	v_readlane_b32 s23, v252, 6
	s_add_i32 s8, 0, 0x10e00
	v_cndmask_b32_e32 v4, v10, v4, vcc
	v_lshlrev_b32_e32 v230, 2, v4
	v_xor_b32_e32 v4, 2, v10
	v_cmp_lt_i32_e32 vcc, v4, v11
	s_lshl_b32 s22, s23, 5
	v_and_b32_e32 v1, 15, v2
	v_cndmask_b32_e32 v4, v10, v4, vcc
	v_lshlrev_b32_e32 v231, 2, v4
	v_xor_b32_e32 v4, 4, v10
	v_bfe_u32 v3, v2, 3, 3
	v_cmp_lt_i32_e32 vcc, v4, v11
	s_add_i32 s6, s8, s22
	s_mov_b32 s21, 0
	v_cndmask_b32_e32 v4, v10, v4, vcc
	v_lshl_add_u32 v233, v3, 2, s6
	s_lshl_b32 s20, s23, 8
	s_lshl_b32 s6, s23, 9
	v_lshlrev_b32_e32 v8, 12, v1
	v_mov_b32_e32 v9, v5
	v_lshlrev_b32_e32 v232, 2, v4
	s_mov_b32 s7, s21
	s_add_u32 s0, s0, s6
	v_and_b32_e32 v4, 48, v2
	v_lshl_add_u64 v[8:9], s[84:85], 0, v[8:9]
	v_cmp_eq_u32_e64 s[4:5], 0, v6
	s_addc_u32 s1, s1, 0
	v_lshlrev_b32_e32 v6, 1, v4
	v_mov_b32_e32 v7, v5
	v_lshl_add_u64 v[8:9], v[8:9], 0, s[6:7]
	v_lshl_add_u64 v[200:201], s[0:1], 0, v[6:7]
	v_lshl_add_u64 v[6:7], v[8:9], 0, v[6:7]
	s_mov_b64 s[0:1], 0x210000
	v_lshl_add_u64 v[202:203], v[6:7], 0, s[0:1]
	s_mov_b64 s[0:1], 0x230000
	v_lshl_add_u64 v[204:205], v[6:7], 0, s[0:1]
	s_lshl_b64 s[0:1], s[20:21], 2
	s_add_u32 s0, s66, s0
	s_addc_u32 s1, s67, s1
	v_lshlrev_b32_e32 v8, 2, v4
	v_mov_b32_e32 v9, v5
	v_lshl_add_u64 v[206:207], s[0:1], 0, v[8:9]
	s_add_u32 s0, s84, s20
	s_addc_u32 s1, s85, 0
	v_lshl_or_b32 v229, s23, 3, v3
	v_lshl_add_u64 v[8:9], s[0:1], 0, v[4:5]
	s_mov_b64 s[0:1], 0x35400000
	v_lshlrev_b32_e32 v3, 2, v1
	v_lshl_add_u64 v[208:209], v[8:9], 0, s[0:1]
	v_add_u32_e32 v234, s8, v3
	s_mov_b64 s[0:1], 0x220000
	v_add_u32_e32 v8, 0, v3
	v_xor_b32_e32 v3, 16, v10
	v_lshl_add_u64 v[210:211], v[6:7], 0, s[0:1]
	s_mov_b64 s[0:1], 0x240000
	v_cmp_lt_i32_e32 vcc, v3, v11
	v_lshl_add_u64 v[212:213], v[6:7], 0, s[0:1]
	v_readlane_b32 s0, v252, 0
	v_cndmask_b32_e32 v3, v10, v3, vcc
	s_and_b32 s0, s0, 0x1ffffc0
	v_lshrrev_b32_e32 v4, 2, v2
	v_lshlrev_b32_e32 v236, 2, v3
	v_xor_b32_e32 v3, 8, v10
	v_and_or_b32 v4, v4, 12, s0
	v_cmp_lt_i32_e32 vcc, v3, v11
	s_movk_i32 s0, 0x100
	v_lshlrev_b32_e32 v6, 6, v2
	v_bfe_u32 v9, v2, 5, 1
	v_and_b32_e32 v235, 31, v2
	v_cndmask_b32_e32 v3, v10, v3, vcc
	v_cmp_gt_i32_e64 s[14:15], 32, v2
	v_cmp_gt_i32_e64 s[16:17], s0, v2
	v_lshlrev_b32_e32 v10, 2, v2
	s_add_i32 s0, 0, 0x10200
	v_ashrrev_i32_e32 v7, 31, v6
	v_ashrrev_i32_e32 v240, 2, v2
	v_lshlrev_b32_e32 v2, 4, v2
	v_lshlrev_b32_e32 v237, 2, v3
	v_add_u32_e32 v239, s0, v10
	v_lshl_add_u64 v[6:7], v[6:7], 2, s[84:85]
	s_mov_b64 s[0:1], 0x8000
	v_and_b32_e32 v2, 48, v2
	v_mov_b32_e32 v3, v5
	v_lshl_add_u64 v[216:217], v[6:7], 0, s[0:1]
	v_lshl_add_u64 v[2:3], s[84:85], 0, v[2:3]
	s_mov_b64 s[0:1], 0x45200000
	v_lshl_add_u64 v[218:219], v[2:3], 0, s[0:1]
	v_lshl_or_b32 v2, v9, 2, s22
	s_add_i32 s0, 0, 0x10600
	v_add_lshl_u32 v242, v2, v235, 2
	v_add_u32_e32 v243, 0x10e00, v2
	v_lshlrev_b32_e32 v2, 7, v9
	v_lshlrev_b32_e32 v12, 7, v4
	v_lshlrev_b32_e32 v4, 2, v235
	s_add_i32 s33, 0, 0x10a00
	v_add_u32_e32 v241, s0, v10
	v_lshl_or_b32 v2, s23, 10, v2
	s_movk_i32 s0, 0x200
	v_cmp_gt_u32_e64 s[6:7], 4, v235
	v_cmp_eq_u32_e64 s[8:9], 0, v235
	v_cmp_eq_u32_e64 s[10:11], 1, v235
	v_cmp_eq_u32_e64 s[12:13], 2, v235
	v_lshl_add_u64 v[214:215], s[70:71], 0, v[4:5]
	v_add_u32_e32 v238, s33, v10
	v_or3_b32 v244, v2, v4, s0
	v_mov_b32_e32 v245, 0x3727c5ac
	s_mov_b64 s[22:23], 0x10000
	s_mov_b32 s40, 0x10000
	s_mov_b64 s[24:25], 0x20000
	s_mov_b32 s41, 0x20000
	s_mov_b64 s[26:27], 0x30000
	s_mov_b32 s42, 0x30000
	s_mov_b64 s[28:29], 0x10080
	s_mov_b64 s[30:31], 0x20080
	s_mov_b64 s[34:35], 0x30080
	s_mov_b32 s43, 0x8000
	s_mov_b32 s44, 0x18000
	v_add_u32_e32 v246, v8, v12
	v_mov_b32_e32 v247, 1
	v_mov_b32_e32 v248, 0xff800000
	s_mov_b32 s45, s96
	v_readlane_b32 s100, v252, 41
	s_nop 3
	s_cmpk_lg_i32 s100, 0x100
	s_cbranch_scc1 .Lmy_p7_nomap
	s_and_b32 s45, s96, 7
	s_lshl_b32 s45, s45, 5
	s_lshr_b32 s100, s96, 3
	s_add_i32 s45, s45, s100
.Lmy_p7_nomap:
	v_readfirstlane_b32 s101, v0
	s_nop 3
	s_lshr_b32 s101, s101, 8
	s_cmp_eq_u32 s101, 0
	s_cbranch_scc1 .Lmy_prio_p7
	s_setprio 1

.LBB0_1265:
	s_setprio 0
	v_readlane_b32 s43, v252, 41
